# hand-off spins (FCNT/YCNT/prologue/ctx): invalidate hoisted before first poll
# speedup vs baseline: 1.0096x; 1.0014x over previous
; __device__ __forceinline__ unsigned xb_ld(unsigned* p)              { return __hip_atomic_load(p, __ATOMIC_RELAXED, __HIP_MEMORY_SCOPE_AGENT); }
; #define XB_SPIN(cond, bar) do { unsigned _sp = 0; while (cond) { __builtin_amdgcn_s_sleep(1); \
;     if ((++_sp & 255u) == 0u) { if (xb_ld(&(bar)[XB_TMO])) break; if (_sp > XB_SPIN_CAP) { atomicAdd(&(bar)[XB_TMO], 1u); break; } } } } while (0)
; template <bool OUTP>
; __device__ __forceinline__ void gemm_phase(const Params& p, int l, char* smem, int vb, int nvb, int pm0, int M, bool fuse, int oz) {
;     ...
;     if (OUTP) {
;         unsigned* bar = (unsigned*)(p.ws + OFF_BAR);
;         __syncthreads();
;         if (threadIdx.x == 0) {
;             XB_SPIN(xb_ld(&bar[XB_FCNT(cur.pm)]) < 256u * (unsigned)(l + 1), bar);
;             __builtin_amdgcn_fence(__ATOMIC_ACQUIRE, "agent");
;             asm volatile("s_waitcnt vmcnt(0)" ::: "memory");
;         }
;         __syncthreads();
;     }
.LBB0_26:
	s_cmp_eq_u32 s77, 3
	s_cselect_b64 s[16:17], -1, 0
	s_andn2_b64 vcc, exec, s[38:39]
	s_cbranch_vccnz .LBB0_142
	v_cndmask_b32_e64 v2, 0, 1, s[36:37]
	s_nop 0
	v_readfirstlane_b32 s1, v2
	s_sub_i32 s1, s77, s1
	s_and_b64 s[24:25], s[36:37], exec
	s_cselect_b32 s2, 64, 0
	s_add_i32 s20, s3, s2
	s_barrier
	s_and_saveexec_b64 s[38:39], s[74:75]
	s_cbranch_execz .LBB0_42
	s_lshl_b32 s24, s20, 6
	s_ashr_i32 s25, s24, 31
	s_lshl_b64 s[24:25], s[24:25], 2
	s_add_u32 s24, s60, s24
	s_addc_u32 s25, s61, s25
	v_mov_b32_e32 v2, 0x75000
	buffer_inv sc1
	global_load_dword v2, v2, s[24:25] offset:1536 sc1
	s_add_u32 s40, s24, 0x75600
	s_addc_u32 s41, s25, 0
	s_lshl_b32 s3, s1, 8
	s_addk_i32 s3, 0x100
	s_waitcnt vmcnt(0)
	v_cmp_le_u32_e32 vcc, s3, v2
	s_cbranch_vccnz .LBB0_41
	s_mov_b32 s24, 1
	s_branch .LBB0_31

; __device__ __forceinline__ unsigned xb_ld(unsigned* p)              { return __hip_atomic_load(p, __ATOMIC_RELAXED, __HIP_MEMORY_SCOPE_AGENT); }
; #define XB_SPIN(cond, bar) do { unsigned _sp = 0; while (cond) { __builtin_amdgcn_s_sleep(1); \
;     if ((++_sp & 255u) == 0u) { if (xb_ld(&(bar)[XB_TMO])) break; if (_sp > XB_SPIN_CAP) { atomicAdd(&(bar)[XB_TMO], 1u); break; } } } } while (0)
; template <bool OUTP>
; __device__ __forceinline__ void gemm_phase(const Params& p, int l, char* smem, int vb, int nvb, int pm0, int M, bool fuse, int oz) {
;     ...
;         if (threadIdx.x == 0) {
;             XB_SPIN(xb_ld(&bar[XB_FCNT(cur.pm)]) < 256u * (unsigned)(l + 1), bar);
;             __builtin_amdgcn_fence(__ATOMIC_ACQUIRE, "agent");
;             asm volatile("s_waitcnt vmcnt(0)" ::: "memory");
;         }
.LBB0_41:
	s_waitcnt vmcnt(0)
	s_waitcnt vmcnt(0)

; __device__ __forceinline__ unsigned xb_ld(unsigned* p)              { return __hip_atomic_load(p, __ATOMIC_RELAXED, __HIP_MEMORY_SCOPE_AGENT); }
; #define XB_SPIN(cond, bar) do { unsigned _sp = 0; while (cond) { __builtin_amdgcn_s_sleep(1); \
;     if ((++_sp & 255u) == 0u) { if (xb_ld(&(bar)[XB_TMO])) break; if (_sp > XB_SPIN_CAP) { atomicAdd(&(bar)[XB_TMO], 1u); break; } } } } while (0)
; __global__ void __launch_bounds__(NT) fwd_megakernel(Params p) {
;     ...
;             if (l >= 1) {
;                 unsigned* bar = (unsigned*)(p.ws + OFF_BAR);
;                 const int r0 = cblk ? (nvb - 32) * 72 + (vb - cgrp) * 8 : vb * 72, r1 = cblk ? r0 + 7 : r0 + 71;
;                 const int pa_ = r0 >> 8, pb_ = ((r1 < LAT) ? r1 : LAT - 1) >> 8;
;                 __syncthreads();
;                 if (threadIdx.x == 0) {
;                     XB_SPIN(xb_ld(&bar[XB_YCNT(pa_)]) < 4u * (unsigned)l, bar);
;                     XB_SPIN(xb_ld(&bar[XB_YCNT(pb_)]) < 4u * (unsigned)l, bar);
;                     __builtin_amdgcn_fence(__ATOMIC_ACQUIRE, "agent");
;                     asm volatile("s_waitcnt vmcnt(0)" ::: "memory");
;                 }
;                 __syncthreads();
;             }
.LBB0_794:
	s_waitcnt vmcnt(0) lgkmcnt(0)
	s_barrier
	s_and_saveexec_b64 s[0:1], s[74:75]
	s_cbranch_execz .LBB0_822
	s_ashr_i32 s2, s3, 2
	s_and_b32 s20, s2, 0xffffffc0
	s_ashr_i32 s21, s20, 31
	s_lshl_b64 s[20:21], s[20:21], 2
	v_readlane_b32 s4, v253, 0
	v_readlane_b32 s5, v253, 1
	s_add_u32 s20, s4, s20
	s_addc_u32 s21, s5, s21
	v_mov_b32_e32 v1, 0xb000
	buffer_inv sc1
	global_load_dword v1, v1, s[20:21] offset:3584 sc1
	s_add_u32 s20, s20, 0xbe00
	s_addc_u32 s21, s21, 0
	s_lshl_b32 s2, s77, 2
	s_waitcnt vmcnt(0)
	v_cmp_le_u32_e32 vcc, s2, v1
	s_cbranch_vccnz .LBB0_808
	s_mov_b32 s25, 1
	s_branch .LBB0_798

; __device__ __forceinline__ unsigned xb_ld(unsigned* p)              { return __hip_atomic_load(p, __ATOMIC_RELAXED, __HIP_MEMORY_SCOPE_AGENT); }
; #define XB_SPIN(cond, bar) do { unsigned _sp = 0; while (cond) { __builtin_amdgcn_s_sleep(1); \
;     if ((++_sp & 255u) == 0u) { if (xb_ld(&(bar)[XB_TMO])) break; if (_sp > XB_SPIN_CAP) { atomicAdd(&(bar)[XB_TMO], 1u); break; } } } } while (0)
; __global__ void __launch_bounds__(NT) fwd_megakernel(Params p) {
;     ...
;             if (l == 0) {
;                 unsigned* bar = (unsigned*)(p.ws + OFF_BAR);
;                 __syncthreads();
;                 if (threadIdx.x == 0) {
;                     XB_SPIN(xb_ld(&bar[193]) < 48u, bar);
;                     __builtin_amdgcn_fence(__ATOMIC_ACQUIRE, "agent");
;                     asm volatile("s_waitcnt vmcnt(0)" ::: "memory");
;                 }
;                 __syncthreads();
;             }
.LBB0_823:
	s_mov_b32 s4, s93
	s_cmp_lg_u32 s77, 0
	s_cbranch_scc1 .LBB0_840
	s_waitcnt vmcnt(0) lgkmcnt(0)
	s_barrier
	s_and_saveexec_b64 s[0:1], s[74:75]
	s_cbranch_execz .LBB0_839
	v_readlane_b32 s2, v253, 58
	v_readlane_b32 s3, v253, 59
	s_nop 4
	buffer_inv sc1
	global_load_dword v1, v3, s[2:3] sc1
	s_waitcnt vmcnt(0)
	v_cmp_lt_u32_e32 vcc, 47, v1
	s_cbranch_vccnz .LBB0_838
	s_mov_b32 s2, 1
	s_branch .LBB0_828

; __device__ __forceinline__ unsigned xb_ld(unsigned* p)              { return __hip_atomic_load(p, __ATOMIC_RELAXED, __HIP_MEMORY_SCOPE_AGENT); }
; #define XB_SPIN(cond, bar) do { unsigned _sp = 0; while (cond) { __builtin_amdgcn_s_sleep(1); \
;     if ((++_sp & 255u) == 0u) { if (xb_ld(&(bar)[XB_TMO])) break; if (_sp > XB_SPIN_CAP) { atomicAdd(&(bar)[XB_TMO], 1u); break; } } } } while (0)
; __device__ void phase_E_rows(const Params& p, int l, char* smem, int vb, int nvb, bool split, int nrows, int oz) {
;     ...
;     } else {
;         unsigned* bar = (unsigned*)(p.ws + OFF_BAR);
;         __syncthreads();
;         if (threadIdx.x == 0) {
;             XB_SPIN(xb_ld(&bar[XB_YCNT(64 + (vb >> 5))]) < 4u * (unsigned)l, bar);
;             __builtin_amdgcn_fence(__ATOMIC_ACQUIRE, "agent");
;             asm volatile("s_waitcnt vmcnt(0)" ::: "memory");
;         }
;         __syncthreads();
.LBB0_843:
	s_andn2_b64 vcc, exec, s[18:19]
	s_mov_b32 s27, s26
	s_mov_b32 s56, s25
	s_cbranch_vccnz .LBB0_861
	s_xor_b64 s[20:21], s[54:55], -1
	s_andn2_b64 vcc, exec, s[20:21]
	s_mov_b32 s56, s58
	s_mov_b32 s27, s24
	s_cbranch_vccnz .LBB0_861
	s_waitcnt lgkmcnt(0)
	s_barrier
	s_and_saveexec_b64 s[20:21], s[74:75]
	s_cbranch_execz .LBB0_860
	buffer_inv sc1
	global_load_dword v2, v3, s[52:53] sc1
	s_waitcnt vmcnt(0)
	v_cmp_le_u32_e32 vcc, s93, v2
	s_cbranch_vccnz .LBB0_859
	s_mov_b32 s27, 1
	s_branch .LBB0_849
